# speedup vs baseline: 1.0043x; 1.0014x over previous
.LBB3_44:
	s_or_b64 exec, exec, s[30:31]
	s_and_saveexec_b64 s[30:31], s[8:9]
	ds_write_b32 v1, v139
	s_or_b64 exec, exec, s[30:31]
	s_add_u32 s34, s18, s6
	s_addc_u32 s35, s19, s7
	s_add_u32 s36, s34, 0x2000
	s_addc_u32 s37, s35, 0
	global_load_dwordx4 v[10:13], v138, s[34:35]
	s_add_u32 s38, s34, 0x4000
	s_addc_u32 s39, s35, 0
	global_load_dwordx4 v[14:17], v138, s[36:37]
	global_load_dwordx4 v[18:21], v138, s[38:39]
	v_add_u32_e32 v35, 0x400, v138
	global_load_dwordx4 v[36:39], v35, s[34:35]
	global_load_dwordx4 v[40:43], v35, s[36:37]
	global_load_dwordx4 v[44:47], v35, s[38:39]
	v_add_u32_e32 v35, 0x800, v138
	global_load_dwordx4 v[48:51], v35, s[34:35]
	global_load_dwordx4 v[52:55], v35, s[36:37]
	global_load_dwordx4 v[56:59], v35, s[38:39]
	v_add_u32_e32 v35, 0xc00, v138
	global_load_dwordx4 v[60:63], v35, s[34:35]
	global_load_dwordx4 v[64:67], v35, s[36:37]
	global_load_dwordx4 v[68:71], v35, s[38:39]
	v_add_u32_e32 v35, 0x1000, v138
	global_load_dwordx4 v[72:75], v35, s[34:35]
	global_load_dwordx4 v[76:79], v35, s[36:37]
	global_load_dwordx4 v[80:83], v35, s[38:39]
	v_add_u32_e32 v35, 0x1400, v138
	global_load_dwordx4 v[84:87], v35, s[34:35]
	global_load_dwordx4 v[88:91], v35, s[36:37]
	global_load_dwordx4 v[92:95], v35, s[38:39]
	v_add_u32_e32 v35, 0x1800, v138
	global_load_dwordx4 v[96:99], v35, s[34:35]
	global_load_dwordx4 v[100:103], v35, s[36:37]
	global_load_dwordx4 v[104:107], v35, s[38:39]
	v_add_u32_e32 v35, 0x1c00, v138
	global_load_dwordx4 v[108:111], v35, s[34:35]
	global_load_dwordx4 v[112:115], v35, s[36:37]
	global_load_dwordx4 v[116:119], v35, s[38:39]
	s_waitcnt vmcnt(23)
	v_sub_f32_e32 v22, v28, v10
	v_mul_f32_e32 v22, v22, v22
	s_waitcnt vmcnt(22)
	v_sub_f32_e32 v23, v29, v14
	s_waitcnt vmcnt(21)
	v_sub_f32_e32 v32, v30, v18
	v_fmac_f32_e32 v22, v23, v23
	v_fmac_f32_e32 v22, v32, v32
	v_cmp_le_f32_e32 vcc, v22, v31
	s_cbranch_vccz .LBB3_50
	s_nop 0
	v_mbcnt_lo_u32_b32 v22, vcc_lo, 0
	v_mbcnt_hi_u32_b32 v22, vcc_hi, v22
	v_cmp_gt_i32_e64 s[6:7], 8, v22
	s_and_b64 s[30:31], vcc, s[6:7]
	s_and_saveexec_b64 s[6:7], s[30:31]
	v_lshl_add_u32 v22, v22, 2, s49
	ds_write_b32 v22, v142
	s_or_b64 exec, exec, s[6:7]
	s_bcnt1_i32_b64 s22, vcc
	s_branch .LBB3_51

.LBB3_79:
	s_waitcnt vmcnt(18)
	v_mov_b32_e32 v10, v36
	v_mov_b32_e32 v11, v37
	v_mov_b32_e32 v12, v38
	v_mov_b32_e32 v13, v39
	v_mov_b32_e32 v14, v40
	v_mov_b32_e32 v15, v41
	v_mov_b32_e32 v16, v42
	v_mov_b32_e32 v17, v43
	v_mov_b32_e32 v18, v44
	v_mov_b32_e32 v19, v45
	v_mov_b32_e32 v20, v46
	v_mov_b32_e32 v21, v47
	v_sub_f32_e32 v32, v28, v10
	v_sub_f32_e32 v33, v29, v14
	v_mul_f32_e32 v32, v32, v32
	v_sub_f32_e32 v34, v30, v18
	v_fmac_f32_e32 v32, v33, v33
	v_fmac_f32_e32 v32, v34, v34
	v_cmp_le_f32_e32 vcc, v32, v31
	s_cbranch_vccz .LBB3_83
	s_nop 0
	v_mbcnt_lo_u32_b32 v32, vcc_lo, 0
	v_mbcnt_hi_u32_b32 v32, vcc_hi, v32
	v_add_u32_e32 v32, s30, v32
	v_cmp_gt_i32_e64 s[6:7], 8, v32
	s_and_b64 s[40:41], vcc, s[6:7]
	s_and_saveexec_b64 s[6:7], s[40:41]
	v_lshl_add_u32 v32, v32, 2, s49
	ds_write_b32 v32, v144
	s_or_b64 exec, exec, s[6:7]
	s_bcnt1_i32_b64 s6, vcc
	s_add_i32 s30, s30, s6

.LBB3_111:
	s_waitcnt vmcnt(15)
	v_mov_b32_e32 v10, v48
	v_mov_b32_e32 v11, v49
	v_mov_b32_e32 v12, v50
	v_mov_b32_e32 v13, v51
	v_mov_b32_e32 v14, v52
	v_mov_b32_e32 v15, v53
	v_mov_b32_e32 v16, v54
	v_mov_b32_e32 v17, v55
	v_mov_b32_e32 v18, v56
	v_mov_b32_e32 v19, v57
	v_mov_b32_e32 v20, v58
	v_mov_b32_e32 v21, v59
	v_sub_f32_e32 v32, v28, v10
	v_sub_f32_e32 v33, v29, v14
	v_mul_f32_e32 v32, v32, v32
	v_sub_f32_e32 v34, v30, v18
	v_fmac_f32_e32 v32, v33, v33
	v_fmac_f32_e32 v32, v34, v34
	v_cmp_le_f32_e32 vcc, v32, v31
	s_cbranch_vccz .LBB3_115
	s_nop 0
	v_mbcnt_lo_u32_b32 v32, vcc_lo, 0
	v_mbcnt_hi_u32_b32 v32, vcc_hi, v32
	v_add_u32_e32 v32, s30, v32
	v_cmp_gt_i32_e64 s[6:7], 8, v32
	s_and_b64 s[40:41], vcc, s[6:7]
	s_and_saveexec_b64 s[6:7], s[40:41]
	v_lshl_add_u32 v32, v32, 2, s49
	ds_write_b32 v32, v146
	s_or_b64 exec, exec, s[6:7]
	s_bcnt1_i32_b64 s6, vcc
	s_add_i32 s30, s30, s6

.LBB3_143:
	s_waitcnt vmcnt(12)
	v_mov_b32_e32 v10, v60
	v_mov_b32_e32 v11, v61
	v_mov_b32_e32 v12, v62
	v_mov_b32_e32 v13, v63
	v_mov_b32_e32 v14, v64
	v_mov_b32_e32 v15, v65
	v_mov_b32_e32 v16, v66
	v_mov_b32_e32 v17, v67
	v_mov_b32_e32 v18, v68
	v_mov_b32_e32 v19, v69
	v_mov_b32_e32 v20, v70
	v_mov_b32_e32 v21, v71
	v_sub_f32_e32 v22, v28, v10
	v_sub_f32_e32 v23, v29, v14
	v_mul_f32_e32 v22, v22, v22
	v_sub_f32_e32 v32, v30, v18
	v_fmac_f32_e32 v22, v23, v23
	v_fmac_f32_e32 v22, v32, v32
	v_cmp_le_f32_e32 vcc, v22, v31
	s_cbranch_vccz .LBB3_147
	s_nop 0
	v_mbcnt_lo_u32_b32 v22, vcc_lo, 0
	v_mbcnt_hi_u32_b32 v22, vcc_hi, v22
	v_add_u32_e32 v22, s30, v22
	v_cmp_gt_i32_e64 s[6:7], 8, v22
	s_and_b64 s[40:41], vcc, s[6:7]
	s_and_saveexec_b64 s[6:7], s[40:41]
	v_lshl_add_u32 v22, v22, 2, s49
	ds_write_b32 v22, v148
	s_or_b64 exec, exec, s[6:7]
	s_bcnt1_i32_b64 s6, vcc
	s_add_i32 s30, s30, s6

.LBB3_175:
	s_waitcnt vmcnt(9)
	v_mov_b32_e32 v10, v72
	v_mov_b32_e32 v11, v73
	v_mov_b32_e32 v12, v74
	v_mov_b32_e32 v13, v75
	v_mov_b32_e32 v14, v76
	v_mov_b32_e32 v15, v77
	v_mov_b32_e32 v16, v78
	v_mov_b32_e32 v17, v79
	v_mov_b32_e32 v18, v80
	v_mov_b32_e32 v19, v81
	v_mov_b32_e32 v20, v82
	v_mov_b32_e32 v21, v83
	v_sub_f32_e32 v22, v28, v10
	v_sub_f32_e32 v23, v29, v14
	v_mul_f32_e32 v22, v22, v22
	v_sub_f32_e32 v32, v30, v18
	v_fmac_f32_e32 v22, v23, v23
	v_fmac_f32_e32 v22, v32, v32
	v_cmp_le_f32_e32 vcc, v22, v31
	s_cbranch_vccz .LBB3_179
	s_nop 0
	v_mbcnt_lo_u32_b32 v22, vcc_lo, 0
	v_mbcnt_hi_u32_b32 v22, vcc_hi, v22
	v_add_u32_e32 v22, s30, v22
	v_cmp_gt_i32_e64 s[6:7], 8, v22
	s_and_b64 s[40:41], vcc, s[6:7]
	s_and_saveexec_b64 s[6:7], s[40:41]
	v_lshl_add_u32 v22, v22, 2, s49
	ds_write_b32 v22, v150
	s_or_b64 exec, exec, s[6:7]
	s_bcnt1_i32_b64 s6, vcc
	s_add_i32 s30, s30, s6

.LBB3_207:
	s_waitcnt vmcnt(6)
	v_mov_b32_e32 v10, v84
	v_mov_b32_e32 v11, v85
	v_mov_b32_e32 v12, v86
	v_mov_b32_e32 v13, v87
	v_mov_b32_e32 v14, v88
	v_mov_b32_e32 v15, v89
	v_mov_b32_e32 v16, v90
	v_mov_b32_e32 v17, v91
	v_mov_b32_e32 v18, v92
	v_mov_b32_e32 v19, v93
	v_mov_b32_e32 v20, v94
	v_mov_b32_e32 v21, v95
	v_sub_f32_e32 v22, v28, v10
	v_sub_f32_e32 v23, v29, v14
	v_mul_f32_e32 v22, v22, v22
	v_sub_f32_e32 v32, v30, v18
	v_fmac_f32_e32 v22, v23, v23
	v_fmac_f32_e32 v22, v32, v32
	v_cmp_le_f32_e32 vcc, v22, v31
	s_cbranch_vccz .LBB3_211
	s_nop 0
	v_mbcnt_lo_u32_b32 v22, vcc_lo, 0
	v_mbcnt_hi_u32_b32 v22, vcc_hi, v22
	v_add_u32_e32 v22, s30, v22
	v_cmp_gt_i32_e64 s[6:7], 8, v22
	s_and_b64 s[40:41], vcc, s[6:7]
	s_and_saveexec_b64 s[6:7], s[40:41]
	v_lshl_add_u32 v22, v22, 2, s49
	ds_write_b32 v22, v152
	s_or_b64 exec, exec, s[6:7]
	s_bcnt1_i32_b64 s6, vcc
	s_add_i32 s30, s30, s6

.LBB3_239:
	s_waitcnt vmcnt(3)
	v_mov_b32_e32 v10, v96
	v_mov_b32_e32 v11, v97
	v_mov_b32_e32 v12, v98
	v_mov_b32_e32 v13, v99
	v_mov_b32_e32 v14, v100
	v_mov_b32_e32 v15, v101
	v_mov_b32_e32 v16, v102
	v_mov_b32_e32 v17, v103
	v_mov_b32_e32 v18, v104
	v_mov_b32_e32 v19, v105
	v_mov_b32_e32 v20, v106
	v_mov_b32_e32 v21, v107
	v_sub_f32_e32 v22, v28, v10
	v_sub_f32_e32 v23, v29, v14
	v_mul_f32_e32 v22, v22, v22
	v_sub_f32_e32 v32, v30, v18
	v_fmac_f32_e32 v22, v23, v23
	v_fmac_f32_e32 v22, v32, v32
	v_cmp_le_f32_e32 vcc, v22, v31
	s_cbranch_vccz .LBB3_243
	s_nop 0
	v_mbcnt_lo_u32_b32 v22, vcc_lo, 0
	v_mbcnt_hi_u32_b32 v22, vcc_hi, v22
	v_add_u32_e32 v22, s30, v22
	v_cmp_gt_i32_e64 s[6:7], 8, v22
	s_and_b64 s[40:41], vcc, s[6:7]
	s_and_saveexec_b64 s[6:7], s[40:41]
	v_lshl_add_u32 v22, v22, 2, s49
	ds_write_b32 v22, v154
	s_or_b64 exec, exec, s[6:7]
	s_bcnt1_i32_b64 s6, vcc
	s_add_i32 s30, s30, s6

.LBB3_271:
	s_waitcnt vmcnt(0)
	v_mov_b32_e32 v10, v108
	v_mov_b32_e32 v11, v109
	v_mov_b32_e32 v12, v110
	v_mov_b32_e32 v13, v111
	v_mov_b32_e32 v14, v112
	v_mov_b32_e32 v15, v113
	v_mov_b32_e32 v16, v114
	v_mov_b32_e32 v17, v115
	v_mov_b32_e32 v18, v116
	v_mov_b32_e32 v19, v117
	v_mov_b32_e32 v20, v118
	v_mov_b32_e32 v21, v119
	v_sub_f32_e32 v22, v28, v10
	v_sub_f32_e32 v23, v29, v14
	v_mul_f32_e32 v22, v22, v22
	v_sub_f32_e32 v32, v30, v18
	v_fmac_f32_e32 v22, v23, v23
	v_fmac_f32_e32 v22, v32, v32
	v_cmp_le_f32_e32 vcc, v22, v31
	s_cbranch_vccz .LBB3_275
	s_nop 0
	v_mbcnt_lo_u32_b32 v22, vcc_lo, 0
	v_mbcnt_hi_u32_b32 v22, vcc_hi, v22
	v_add_u32_e32 v22, s30, v22
	v_cmp_gt_i32_e64 s[6:7], 8, v22
	s_and_b64 s[34:35], vcc, s[6:7]
	s_and_saveexec_b64 s[6:7], s[34:35]
	v_lshl_add_u32 v22, v22, 2, s49
	ds_write_b32 v22, v156
	s_or_b64 exec, exec, s[6:7]
	s_bcnt1_i32_b64 s6, vcc
	s_add_i32 s30, s30, s6
